# P2 states: the waves of SIMDs 2,3 run the two independent halves of a head iteration (MFMAs of head j | conv of head j+1) in the opposite order, from a second copy of the loop body
# baseline (speedup 1.0000x reference)
.LBB0_401:
	s_or_b64 exec, exec, s[38:39]
	v_mul_f32_e64 v32, v29, -v35
	ds_bpermute_b32 v33, v96, v32
	v_or_b32_e32 v125, s42, v69
	v_cmp_eq_u32_e32 vcc, 0, v125
	s_and_b32 s43, s54, 7
	s_lshl_b32 s38, s43, 9
	s_waitcnt lgkmcnt(0)
	v_fma_f32 v33, v29, -v35, v33
	v_cndmask_b32_e64 v32, v33, v32, s[0:1]
	ds_bpermute_b32 v33, v97, v32
	s_waitcnt vmcnt(26)
	v_cndmask_b32_e64 v20, v20, 0, vcc
	s_waitcnt vmcnt(25)
	v_cndmask_b32_e64 v126, v30, 0, vcc
	s_waitcnt vmcnt(24)
	v_cndmask_b32_e64 v134, v31, 0, vcc
	v_lshlrev_b32_e32 v30, 16, v20
	s_waitcnt lgkmcnt(0)
	v_add_f32_e32 v33, v32, v33
	v_cndmask_b32_e64 v32, v33, v32, s[14:15]
	ds_bpermute_b32 v33, v98, v32
	v_and_b32_e32 v31, 0xffff0000, v20
	s_waitcnt vmcnt(0)
	v_fma_f32 v128, v4, v30, v6
	v_or_b32_e32 v35, s38, v1
	v_readlane_b32 s60, v253, 18
	s_waitcnt lgkmcnt(0)
	v_add_f32_e32 v33, v32, v33
	v_cndmask_b32_e64 v32, v33, v32, s[4:5]
	ds_bpermute_b32 v33, v99, v32
	v_readlane_b32 s70, v253, 28
	v_readlane_b32 s71, v253, 29
	v_fma_f32 v135, v5, v31, v7
	v_lshlrev_b32_e32 v125, 16, v126
	s_waitcnt lgkmcnt(0)
	v_add_f32_e32 v20, v32, v33
	v_cndmask_b32_e64 v32, v20, v32, s[6:7]
	ds_bpermute_b32 v33, v100, v32
	v_lshlrev_b32_e32 v20, 2, v35
	v_lshlrev_b32_e32 v130, 16, v122
	v_lshlrev_b32_e32 v131, 16, v134
	v_fmac_f32_e32 v128, v8, v125
	s_waitcnt lgkmcnt(0)
	v_add_f32_e32 v30, v32, v33
	v_cndmask_b32_e64 v127, v30, v32, s[8:9]
	ds_bpermute_b32 v129, v101, v127
	v_lshl_add_u64 v[30:31], s[30:31], 0, v[20:21]
	v_lshl_add_u64 v[32:33], s[70:71], 0, v[20:21]
	v_lshrrev_b32_e32 v220, 5, v0
	v_and_b32_e32 v221, 7, v220
	v_lshrrev_b32_e32 v220, 3, v220
	v_lshlrev_b32_e32 v222, 8, v221
	v_mul_u32_u24_e32 v224, 0x12000, v220
	v_add_u32_e32 v224, v224, v222
	v_mov_b32_e32 v225, 0
	v_mov_b32_e32 v229, 0
	v_lshl_add_u64 v[226:227], v[32:33], 0, v[224:225]
	global_load_dwordx2 v[234:235], v[226:227], off
	v_sub_u32_e32 v223, 1, v220
	v_mul_u32_u24_e32 v228, 0xc000, v223
	v_lshl_add_u64 v[226:227], v[226:227], 0, v[228:229]
	global_load_dwordx2 v[236:237], v[226:227], off
	v_cmp_eq_u32_e64 s[76:77], 1, v220
	v_mul_u32_u24_e32 v228, 0x6000, v223
	v_add_u32_e32 v228, v228, v222
	v_lshlrev_b32_e32 v231, 8, v220
	v_sub_u32_e32 v228, v228, v231
	v_ashrrev_i32_e32 v229, 31, v228
	v_cndmask_b32_e64 v226, v32, v30, s[76:77]
	v_cndmask_b32_e64 v227, v33, v31, s[76:77]
	v_lshl_add_u64 v[226:227], v[226:227], 0, v[228:229]
	global_load_dwordx2 v[238:239], v[226:227], off
	v_and_b32_e32 v230, 31, v0
	v_lshlrev_b32_e32 v230, 3, v230
	v_mul_u32_u24_e32 v231, 0x500, v221
	v_add_u32_e32 v230, v230, v231
	v_add_u32_e32 v230, 0x1b800, v230
	v_mul_u32_u24_e32 v231, 0x300, v220
	v_add_u32_e32 v232, v230, v231
	v_lshl_add_u32 v233, v220, 8, v230
	v_lshlrev_b32_e32 v20, 1, v35
	v_and_b32_e32 v122, 0xffff0000, v122
	s_waitcnt lgkmcnt(0)
	v_add_f32_e32 v35, v127, v129
	v_cndmask_b32_e64 v35, v35, v127, s[10:11]
	v_add_f32_e32 v34, v35, v34
	ds_write2st64_b32 v84, v29, v34 offset0:1 offset1:17
	v_mov_b32_e32 v34, v36
	v_mov_b32_e32 v35, v2
	v_pk_mul_f32 v[132:133], v[34:35], v[130:131]
	v_and_b32_e32 v127, 0xffff0000, v126
	v_add_f32_e32 v2, v133, v128
	v_add_f32_e32 v29, v132, v2
	v_mul_f32_e32 v2, 0xbfb8aa3b, v29
	v_exp_f32_e32 v2, v2
	v_lshlrev_b32_e32 v129, 16, v123
	v_lshlrev_b32_e32 v128, 16, v124
	v_and_b32_e32 v133, 0xffff0000, v123
	v_add_f32_e32 v2, 1.0, v2
	v_and_b32_e32 v132, 0xffff0000, v124
	v_rcp_f32_e32 v124, v2
	v_and_b32_e32 v123, 0xffff0000, v134
	v_mov_b32_e32 v2, v37
	v_fmac_f32_e32 v135, v9, v127
	v_pk_mul_f32 v[36:37], v[2:3], v[122:123]
	v_mul_f32_e32 v29, v29, v124
	v_add_f32_e32 v37, v37, v135
	v_add_f32_e32 v126, v36, v37
	v_mul_f32_e32 v36, 0xbfb8aa3b, v126
	v_exp_f32_e32 v134, v36
	v_mov_b32_e32 v37, v4
	v_mov_b32_e32 v36, v8
	v_mov_b32_e32 v124, v131
	v_add_f32_e32 v4, 1.0, v134
	v_rcp_f32_e32 v4, v4
	v_pk_mul_f32 v[124:125], v[36:37], v[124:125]
	v_pk_mul_f32 v[134:135], v[36:37], v[130:131]
	v_add_f32_e32 v125, v125, v6
	v_mul_f32_e32 v138, v126, v4
	v_mov_b32_e32 v4, v9
	v_mov_b32_e32 v126, v123
	v_pk_mul_f32 v[8:9], v[4:5], v[126:127]
	v_pk_mov_b32 v[126:127], v[128:129], v[130:131] op_sel:[1,0]
	v_add_f32_e32 v124, v124, v125
	v_pk_mul_f32 v[130:131], v[34:35], v[126:127]
	v_add_f32_e32 v135, v135, v6
	v_add_f32_e32 v124, v131, v124
	v_add_f32_e32 v139, v130, v124
	v_mul_f32_e32 v124, 0xbfb8aa3b, v139
	v_exp_f32_e32 v136, v124
	v_add_f32_e32 v134, v134, v135
	v_lshlrev_b32_e32 v131, 16, v120
	v_and_b32_e32 v135, 0xffff0000, v120
	v_add_f32_e32 v136, 1.0, v136
	v_rcp_f32_e32 v140, v136
	v_pk_mul_f32 v[136:137], v[34:35], v[128:129]
	v_lshlrev_b32_e32 v130, 16, v121
	v_add_f32_e32 v134, v137, v134
	v_add_f32_e32 v136, v136, v134
	v_mul_f32_e32 v134, 0xbfb8aa3b, v136
	v_exp_f32_e32 v137, v134
	v_and_b32_e32 v134, 0xffff0000, v121
	v_add_f32_e32 v9, v9, v7
	v_pk_mul_f32 v[124:125], v[4:5], v[122:123]
	v_add_f32_e32 v120, 1.0, v137
	v_rcp_f32_e32 v137, v120
	v_pk_mov_b32 v[120:121], v[132:133], v[122:123] op_sel:[1,0]
	v_add_f32_e32 v8, v8, v9
	v_pk_mul_f32 v[122:123], v[2:3], v[120:121]
	v_mul_f32_e32 v139, v139, v140
	v_add_f32_e32 v8, v123, v8
	v_add_f32_e32 v140, v122, v8
	v_mul_f32_e32 v8, 0xbfb8aa3b, v140
	v_add_f32_e32 v123, v125, v7
	v_exp_f32_e32 v122, v8
	v_pk_mul_f32 v[8:9], v[2:3], v[132:133]
	v_add_f32_e32 v123, v124, v123
	v_add_f32_e32 v9, v9, v123
	v_add_f32_e32 v124, v8, v9
	v_mul_f32_e32 v8, 0xbfb8aa3b, v124
	v_exp_f32_e32 v8, v8
	v_add_f32_e32 v9, 1.0, v122
	v_mul_f32_e32 v136, v136, v137
	v_rcp_f32_e32 v125, v9
	v_add_f32_e32 v8, 1.0, v8
	v_rcp_f32_e32 v137, v8
	v_pk_mul_f32 v[8:9], v[36:37], v[126:127]
	v_mul_f32_e32 v140, v140, v125
	v_add_f32_e32 v9, v9, v6
	v_mul_f32_e32 v137, v124, v137
	v_pk_mov_b32 v[124:125], v[130:131], v[128:129] op_sel:[1,0]
	v_add_f32_e32 v8, v8, v9
	v_pk_mul_f32 v[126:127], v[34:35], v[124:125]
	v_pk_mul_f32 v[122:123], v[36:37], v[128:129]
	v_add_f32_e32 v8, v127, v8
	v_add_f32_e32 v141, v126, v8
	v_mul_f32_e32 v8, 0xbfb8aa3b, v141
	v_exp_f32_e32 v128, v8
	v_add_f32_e32 v123, v123, v6
	v_add_f32_e32 v122, v122, v123
	v_pk_mul_f32 v[120:121], v[4:5], v[120:121]
	v_add_f32_e32 v128, 1.0, v128
	v_rcp_f32_e32 v142, v128
	v_pk_mul_f32 v[128:129], v[34:35], v[130:131]
	v_lshlrev_b32_e32 v127, 16, v118
	v_add_f32_e32 v122, v129, v122
	v_add_f32_e32 v143, v128, v122
	v_mul_f32_e32 v122, 0xbfb8aa3b, v143
	v_exp_f32_e32 v128, v122
	v_and_b32_e32 v123, 0xffff0000, v118
	v_lshlrev_b32_e32 v126, 16, v119
	v_and_b32_e32 v122, 0xffff0000, v119
	v_add_f32_e32 v118, 1.0, v128
	v_mul_f32_e32 v141, v141, v142
	v_rcp_f32_e32 v142, v118
	v_pk_mov_b32 v[118:119], v[134:135], v[132:133] op_sel:[1,0]
	v_add_f32_e32 v121, v121, v7
	v_pk_mul_f32 v[128:129], v[2:3], v[118:119]
	v_add_f32_e32 v120, v120, v121
	v_add_f32_e32 v120, v129, v120
	v_pk_mul_f32 v[8:9], v[4:5], v[132:133]
	v_add_f32_e32 v132, v128, v120
	v_mul_f32_e32 v120, 0xbfb8aa3b, v132
	v_exp_f32_e32 v128, v120
	v_add_f32_e32 v9, v9, v7
	v_add_f32_e32 v8, v8, v9
	v_mul_f32_e32 v142, v143, v142
	v_add_f32_e32 v128, 1.0, v128
	v_rcp_f32_e32 v133, v128
	v_pk_mul_f32 v[128:129], v[2:3], v[134:135]
	v_pk_mul_f32 v[120:121], v[36:37], v[124:125]
	v_add_f32_e32 v8, v129, v8
	v_add_f32_e32 v143, v128, v8
	v_mul_f32_e32 v8, 0xbfb8aa3b, v143
	v_exp_f32_e32 v144, v8
	v_pk_mov_b32 v[8:9], v[126:127], v[130:131] op_sel:[1,0]
	v_add_f32_e32 v121, v121, v6
	v_pk_mul_f32 v[128:129], v[34:35], v[8:9]
	v_add_f32_e32 v120, v120, v121
	v_add_f32_e32 v120, v129, v120
	v_add_f32_e32 v128, v128, v120
	v_mul_f32_e32 v120, 0xbfb8aa3b, v128
	v_exp_f32_e32 v120, v120
	v_pk_mul_f32 v[118:119], v[4:5], v[118:119]
	v_pk_mul_f32 v[124:125], v[36:37], v[130:131]
	v_pk_mov_b32 v[130:131], v[122:123], v[134:135] op_sel:[1,0]
	v_add_f32_e32 v120, 1.0, v120
	v_rcp_f32_e32 v129, v120
	v_add_f32_e32 v119, v119, v7
	v_add_f32_e32 v121, 1.0, v144
	v_mul_f32_e32 v144, v132, v133
	v_pk_mul_f32 v[132:133], v[2:3], v[130:131]
	v_add_f32_e32 v118, v118, v119
	v_add_f32_e32 v118, v133, v118
	v_mul_f32_e32 v145, v128, v129
	v_pk_mul_f32 v[128:129], v[34:35], v[126:127]
	v_add_f32_e32 v127, v132, v118
	v_rcp_f32_e32 v121, v121
	v_mul_f32_e32 v118, 0xbfb8aa3b, v127
	v_exp_f32_e32 v118, v118
	v_add_f32_e32 v125, v125, v6
	v_mul_f32_e32 v143, v143, v121
	v_pk_mul_f32 v[120:121], v[4:5], v[134:135]
	v_add_f32_e32 v119, v124, v125
	v_add_f32_e32 v119, v129, v119
	v_add_f32_e32 v118, 1.0, v118
	v_add_f32_e32 v121, v121, v7
	v_add_f32_e32 v124, v128, v119
	v_rcp_f32_e32 v125, v118
	v_pk_mul_f32 v[118:119], v[2:3], v[122:123]
	v_add_f32_e32 v120, v120, v121
	v_add_f32_e32 v119, v119, v120
	v_add_f32_e32 v123, v118, v119
	v_mul_f32_e32 v118, 0xbfb8aa3b, v124
	v_exp_f32_e32 v118, v118
	v_mul_f32_e32 v119, 0xbfb8aa3b, v123
	v_exp_f32_e32 v119, v119
	v_pk_mul_f32 v[8:9], v[36:37], v[8:9]
	v_lshlrev_b32_e32 v120, 16, v117
	v_mov_b32_e32 v121, v126
	v_add_f32_e32 v9, v9, v6
	v_add_f32_e32 v118, 1.0, v118
	v_pk_mul_f32 v[120:121], v[34:35], v[120:121]
	v_add_f32_e32 v8, v8, v9
	v_mul_f32_e32 v125, v127, v125
	v_rcp_f32_e32 v127, v118
	v_add_f32_e32 v128, 1.0, v119
	v_pk_mul_f32 v[118:119], v[4:5], v[130:131]
	v_add_f32_e32 v8, v121, v8
	v_add_f32_e32 v120, v120, v8
	v_and_b32_e32 v8, 0xffff0000, v117
	v_mov_b32_e32 v9, v122
	v_add_f32_e32 v117, v119, v7
	v_pk_mul_f32 v[8:9], v[2:3], v[8:9]
	v_add_f32_e32 v117, v118, v117
	v_add_f32_e32 v9, v9, v117
	v_add_f32_e32 v8, v8, v9
	v_mul_f32_e32 v9, 0xbfb8aa3b, v120
	v_mul_f32_e32 v117, 0xbfb8aa3b, v8
	v_exp_f32_e32 v9, v9
	v_exp_f32_e32 v117, v117
	v_rcp_f32_e32 v118, v128
	v_mul_f32_e32 v121, v124, v127
	v_add_f32_e32 v9, 1.0, v9
	v_add_f32_e32 v117, 1.0, v117
	v_rcp_f32_e32 v9, v9
	v_rcp_f32_e32 v117, v117
	v_mul_f32_e32 v126, v123, v118
	v_cvt_pk_bf16_f32 v118, v29, v139
	v_mul_f32_e32 v9, v120, v9
	v_mul_f32_e32 v8, v8, v117
	v_cvt_pk_bf16_f32 v119, v136, v141
	v_cvt_pk_bf16_f32 v120, v142, v145
	v_cvt_pk_bf16_f32 v121, v121, v9
	v_cvt_pk_bf16_f32 v122, v138, v140
	v_cvt_pk_bf16_f32 v123, v137, v144
	v_cvt_pk_bf16_f32 v124, v143, v125
	v_cvt_pk_bf16_f32 v125, v126, v8
	v_lshlrev_b32_e32 v8, 16, v116
	v_lshlrev_b32_e32 v9, 16, v113
	ds_write_b128 v85, v[118:121] offset:8192
	ds_write_b128 v85, v[122:125] offset:8464
	v_pk_mul_f32 v[118:119], v[36:37], v[8:9]
	v_lshlrev_b32_e32 v123, 16, v114
	v_lshlrev_b32_e32 v122, 16, v57
	v_add_f32_e32 v9, v119, v6
	v_pk_mul_f32 v[126:127], v[34:35], v[122:123]
	v_add_f32_e32 v9, v118, v9
	v_add_f32_e32 v9, v127, v9
	v_and_b32_e32 v117, 0xffff0000, v113
	v_and_b32_e32 v116, 0xffff0000, v116
	v_add_f32_e32 v9, v126, v9
	v_pk_mul_f32 v[120:121], v[4:5], v[116:117]
	v_mul_f32_e32 v29, 0xbfb8aa3b, v9
	v_and_b32_e32 v125, 0xffff0000, v114
	v_exp_f32_e32 v29, v29
	v_and_b32_e32 v124, 0xffff0000, v57
	v_add_f32_e32 v57, v121, v7
	v_pk_mul_f32 v[126:127], v[2:3], v[124:125]
	v_add_f32_e32 v57, v120, v57
	v_add_f32_e32 v57, v127, v57
	v_add_f32_e32 v57, v126, v57
	v_add_f32_e32 v29, 1.0, v29
	v_mul_f32_e32 v113, 0xbfb8aa3b, v57
	v_rcp_f32_e32 v29, v29
	v_exp_f32_e32 v114, v113
	v_lshlrev_b32_e32 v119, 16, v112
	v_lshlrev_b32_e32 v118, 16, v115
	v_mul_f32_e32 v29, v9, v29
	v_add_f32_e32 v9, 1.0, v114
	v_rcp_f32_e32 v120, v9
	v_pk_mov_b32 v[8:9], v[122:123], v[8:9] op_sel:[1,0]
	v_and_b32_e32 v113, 0xffff0000, v112
	v_pk_mul_f32 v[8:9], v[36:37], v[8:9]
	v_mul_f32_e32 v128, v57, v120
	v_pk_mov_b32 v[120:121], v[118:119], v[122:123] op_sel:[1,0]
	v_add_f32_e32 v9, v9, v6
	v_and_b32_e32 v112, 0xffff0000, v115
	v_pk_mul_f32 v[114:115], v[36:37], v[122:123]
	v_pk_mul_f32 v[122:123], v[34:35], v[120:121]
	v_add_f32_e32 v8, v8, v9
	v_add_f32_e32 v8, v123, v8
	v_add_f32_e32 v129, v122, v8
	v_mul_f32_e32 v8, 0xbfb8aa3b, v129
	v_exp_f32_e32 v57, v8
	v_pk_mul_f32 v[126:127], v[34:35], v[118:119]
	v_pk_mov_b32 v[116:117], v[124:125], v[116:117] op_sel:[1,0]
	v_lshlrev_b32_e32 v123, 16, v55
	v_add_f32_e32 v57, 1.0, v57
	v_rcp_f32_e32 v130, v57
	v_add_f32_e32 v57, v115, v6
	v_add_f32_e32 v57, v114, v57
	v_add_f32_e32 v57, v127, v57
	v_add_f32_e32 v126, v126, v57
	v_mul_f32_e32 v57, 0xbfb8aa3b, v126
	v_exp_f32_e32 v114, v57
	v_pk_mul_f32 v[116:117], v[4:5], v[116:117]
	v_and_b32_e32 v57, 0xffff0000, v55
	v_add_f32_e32 v117, v117, v7
	v_add_f32_e32 v55, 1.0, v114
	v_pk_mov_b32 v[114:115], v[112:113], v[124:125] op_sel:[1,0]
	v_pk_mul_f32 v[8:9], v[4:5], v[124:125]
	v_pk_mul_f32 v[124:125], v[2:3], v[114:115]
	v_add_f32_e32 v116, v116, v117
	v_add_f32_e32 v116, v125, v116
	v_add_f32_e32 v124, v124, v116
	v_mul_f32_e32 v116, 0xbfb8aa3b, v124
	v_add_f32_e32 v9, v9, v7
	v_exp_f32_e32 v125, v116
	v_pk_mul_f32 v[116:117], v[2:3], v[112:113]
	v_add_f32_e32 v8, v8, v9
	v_add_f32_e32 v8, v117, v8
	v_mul_f32_e32 v127, v129, v130
	v_add_f32_e32 v129, v116, v8
	v_mul_f32_e32 v8, 0xbfb8aa3b, v129
	v_exp_f32_e32 v8, v8
	v_rcp_f32_e32 v55, v55
	v_add_f32_e32 v9, 1.0, v125
	v_lshlrev_b32_e32 v122, 16, v56
	v_add_f32_e32 v8, 1.0, v8
	v_mul_f32_e32 v126, v126, v55
	v_rcp_f32_e32 v55, v9
	v_rcp_f32_e32 v125, v8
	v_pk_mul_f32 v[8:9], v[36:37], v[120:121]
	v_pk_mul_f32 v[116:117], v[36:37], v[118:119]
	v_pk_mov_b32 v[118:119], v[122:123], v[118:119] op_sel:[1,0]
	v_add_f32_e32 v9, v9, v6
	v_pk_mul_f32 v[120:121], v[34:35], v[118:119]
	v_add_f32_e32 v8, v8, v9
	v_add_f32_e32 v8, v121, v8
	v_add_f32_e32 v131, v120, v8
	v_mul_f32_e32 v8, 0xbfb8aa3b, v131
	v_mul_f32_e32 v130, v124, v55
	v_exp_f32_e32 v55, v8
	v_mul_f32_e32 v129, v129, v125
	v_pk_mul_f32 v[124:125], v[34:35], v[122:123]
	v_and_b32_e32 v56, 0xffff0000, v56
	v_add_f32_e32 v55, 1.0, v55
	v_rcp_f32_e32 v132, v55
	v_add_f32_e32 v55, v117, v6
	v_add_f32_e32 v55, v116, v55
	v_add_f32_e32 v55, v125, v55
	v_add_f32_e32 v124, v124, v55
	v_mul_f32_e32 v55, 0xbfb8aa3b, v124
	v_exp_f32_e32 v116, v55
	v_pk_mul_f32 v[114:115], v[4:5], v[114:115]
	v_pk_mul_f32 v[8:9], v[4:5], v[112:113]
	v_pk_mov_b32 v[112:113], v[56:57], v[112:113] op_sel:[1,0]
	v_add_f32_e32 v116, 1.0, v116
	v_add_f32_e32 v115, v115, v7
	v_rcp_f32_e32 v125, v116
	v_pk_mul_f32 v[116:117], v[2:3], v[112:113]
	v_add_f32_e32 v114, v114, v115
	v_add_f32_e32 v114, v117, v114
	v_lshlrev_b32_e32 v121, 16, v53
	v_and_b32_e32 v55, 0xffff0000, v53
	v_mul_f32_e32 v53, v131, v132
	v_add_f32_e32 v131, v116, v114
	v_mul_f32_e32 v114, 0xbfb8aa3b, v131
	v_exp_f32_e32 v132, v114
	v_pk_mul_f32 v[114:115], v[36:37], v[118:119]
	v_add_f32_e32 v9, v9, v7
	v_mul_f32_e32 v124, v124, v125
	v_add_f32_e32 v118, 1.0, v132
	v_rcp_f32_e32 v125, v118
	v_pk_mul_f32 v[118:119], v[2:3], v[56:57]
	v_add_f32_e32 v8, v8, v9
	v_add_f32_e32 v8, v119, v8
	v_add_f32_e32 v132, v118, v8
	v_lshlrev_b32_e32 v120, 16, v54
	v_mul_f32_e32 v8, 0xbfb8aa3b, v132
	v_exp_f32_e32 v133, v8
	v_pk_mov_b32 v[8:9], v[120:121], v[122:123] op_sel:[1,0]
	v_add_f32_e32 v115, v115, v6
	v_pk_mul_f32 v[118:119], v[34:35], v[8:9]
	v_add_f32_e32 v114, v114, v115
	v_add_f32_e32 v114, v119, v114
	v_add_f32_e32 v118, v118, v114
	v_mul_f32_e32 v114, 0xbfb8aa3b, v118
	v_exp_f32_e32 v114, v114
	v_add_f32_e32 v115, 1.0, v133
	v_rcp_f32_e32 v115, v115
	v_and_b32_e32 v54, 0xffff0000, v54
	v_add_f32_e32 v114, 1.0, v114
	v_rcp_f32_e32 v119, v114
	v_pk_mul_f32 v[112:113], v[4:5], v[112:113]
	v_mul_f32_e32 v125, v131, v125
	v_mul_f32_e32 v131, v132, v115
	v_pk_mul_f32 v[114:115], v[4:5], v[56:57]
	v_pk_mov_b32 v[56:57], v[54:55], v[56:57] op_sel:[1,0]
	v_add_f32_e32 v113, v113, v7
	v_pk_mul_f32 v[116:117], v[36:37], v[122:123]
	v_pk_mul_f32 v[122:123], v[2:3], v[56:57]
	v_add_f32_e32 v112, v112, v113
	v_add_f32_e32 v112, v123, v112
	v_mul_f32_e32 v132, v118, v119
	v_pk_mul_f32 v[118:119], v[34:35], v[120:121]
	v_add_f32_e32 v121, v122, v112
	v_mul_f32_e32 v112, 0xbfb8aa3b, v121
	v_exp_f32_e32 v112, v112
	v_add_f32_e32 v117, v117, v6
	v_add_f32_e32 v113, v116, v117
	v_add_f32_e32 v113, v119, v113
	v_add_f32_e32 v112, 1.0, v112
	v_pk_mul_f32 v[8:9], v[36:37], v[8:9]
	v_add_f32_e32 v116, v118, v113
	v_rcp_f32_e32 v117, v112
	v_pk_mul_f32 v[112:113], v[2:3], v[54:55]
	v_add_f32_e32 v55, v115, v7
	v_pk_mul_f32 v[4:5], v[4:5], v[56:57]
	v_lshlrev_b32_e32 v36, 16, v52
	v_mov_b32_e32 v37, v120
	v_add_f32_e32 v6, v9, v6
	v_add_f32_e32 v55, v114, v55
	v_pk_mul_f32 v[34:35], v[34:35], v[36:37]
	v_add_f32_e32 v6, v8, v6
	v_and_b32_e32 v8, 0xffff0000, v52
	v_mov_b32_e32 v9, v54
	v_add_f32_e32 v5, v5, v7
	v_add_f32_e32 v55, v113, v55
	v_add_f32_e32 v6, v35, v6
	v_pk_mul_f32 v[2:3], v[2:3], v[8:9]
	v_add_f32_e32 v4, v4, v5
	v_add_f32_e32 v55, v112, v55
	v_add_f32_e32 v6, v34, v6
	v_add_f32_e32 v3, v3, v4
	v_mul_f32_e32 v112, 0xbfb8aa3b, v116
	v_mul_f32_e32 v113, 0xbfb8aa3b, v55
	v_add_f32_e32 v2, v2, v3
	v_mul_f32_e32 v3, 0xbfb8aa3b, v6
	v_exp_f32_e32 v112, v112
	v_exp_f32_e32 v113, v113
	v_exp_f32_e32 v3, v3
	v_mul_f32_e32 v4, 0xbfb8aa3b, v2
	v_exp_f32_e32 v4, v4
	v_add_f32_e32 v112, 1.0, v112
	v_add_f32_e32 v113, 1.0, v113
	v_add_f32_e32 v3, 1.0, v3
	v_rcp_f32_e32 v112, v112
	v_rcp_f32_e32 v5, v113
	v_rcp_f32_e32 v3, v3
	v_add_f32_e32 v4, 1.0, v4
	v_rcp_f32_e32 v4, v4
	v_mul_f32_e32 v7, v116, v112
	v_mul_f32_e32 v9, v55, v5
	v_mul_f32_e32 v5, v6, v3
	v_mul_f32_e32 v114, v121, v117
	v_mul_f32_e32 v34, v2, v4
	v_cvt_pk_bf16_f32 v2, v29, v127
	v_cvt_pk_bf16_f32 v3, v126, v53
	v_cvt_pk_bf16_f32 v4, v124, v132
	v_cvt_pk_bf16_f32 v5, v7, v5
	v_cvt_pk_bf16_f32 v6, v128, v130
	v_cvt_pk_bf16_f32 v7, v129, v125
	v_cvt_pk_bf16_f32 v8, v131, v114
	v_cvt_pk_bf16_f32 v9, v9, v34
	ds_write_b128 v85, v[2:5] offset:8320
	ds_write_b128 v85, v[6:9] offset:8592
	s_waitcnt lgkmcnt(0)
	s_barrier
	v_cndmask_b32_e64 v3, v50, 0, s[12:13]
	v_cndmask_b32_e64 v9, v51, 0, s[12:13]
	ds_read_b32 v29, v21 offset:4604
	ds_read_b128 v[50:53], v86 offset:4096
	v_cndmask_b32_e64 v2, v49, 0, s[12:13]
	v_lshlrev_b32_e32 v4, 16, v2
	v_fma_f32 v36, v12, v4, v14
	v_lshlrev_b32_e32 v37, 16, v3
	s_waitcnt lgkmcnt(0)
	v_sub_f32_e32 v34, v29, v50
	v_mul_f32_e32 v34, 0x3fb8aa3b, v34
	v_exp_f32_e32 v113, v34
	v_lshlrev_b32_e32 v117, 16, v9
	v_lshlrev_b32_e32 v116, 16, v45
	v_mov_b32_e32 v34, v18
	v_mov_b32_e32 v35, v10
	v_fmac_f32_e32 v36, v16, v37
	v_pk_mul_f32 v[118:119], v[34:35], v[116:117]
	v_and_b32_e32 v2, 0xffff0000, v2
	v_add_f32_e32 v10, v119, v36
	v_add_f32_e32 v10, v118, v10
	v_mul_f32_e32 v18, 0xbfb8aa3b, v10
	v_exp_f32_e32 v18, v18
	v_fma_f32 v57, v13, v2, v15
	v_and_b32_e32 v49, 0xffff0000, v3
	v_lshlrev_b32_e32 v115, 16, v46
	v_add_f32_e32 v18, 1.0, v18
	v_rcp_f32_e32 v18, v18
	v_and_b32_e32 v119, 0xffff0000, v46
	v_and_b32_e32 v121, 0xffff0000, v9
	v_and_b32_e32 v120, 0xffff0000, v45
	v_mul_f32_e32 v46, v10, v18
	v_mov_b32_e32 v10, v19
	v_fmac_f32_e32 v57, v17, v49
	v_pk_mul_f32 v[18:19], v[10:11], v[120:121]
	ds_read_b128 v[2:5], v86
	ds_read_b96 v[6:8], v86 offset:16
	ds_read_b96 v[54:56], v86 offset:4112
	v_add_f32_e32 v9, v19, v57
	v_add_f32_e32 v18, v18, v9
	v_mul_f32_e32 v9, 0xbfb8aa3b, v18
	v_exp_f32_e32 v9, v9
	v_sub_f32_e32 v36, v29, v51
	v_lshlrev_b32_e32 v114, 16, v48
	v_and_b32_e32 v118, 0xffff0000, v48
	v_add_f32_e32 v9, 1.0, v9
	v_rcp_f32_e32 v112, v9
	v_mul_f32_e32 v36, 0x3fb8aa3b, v36
	v_mov_b32_e32 v123, v12
	s_waitcnt lgkmcnt(2)
	v_mov_b32_e32 v19, v2
	v_mov_b32_e32 v12, v17
	v_mov_b32_e32 v48, v121
	v_fma_f32 v2, v13, v49, v15
	v_exp_f32_e32 v51, v36
	v_mov_b32_e32 v122, v16
	v_mov_b32_e32 v36, v117
	v_pk_mul_f32 v[18:19], v[18:19], v[112:113]
	v_pk_fma_f32 v[16:17], v[12:13], v[48:49], v[2:3] op_sel_hi:[1,1,0]
	v_fma_f32 v2, v13, v121, v15
	v_pk_mul_f32 v[36:37], v[122:123], v[36:37]
	v_mul_f32_e32 v57, v46, v19
	v_mul_f32_e32 v126, v18, v19
	v_pk_fma_f32 v[18:19], v[12:13], v[120:121], v[2:3] op_sel_hi:[1,1,0]
	v_sub_f32_e32 v2, v29, v52
	v_mul_f32_e32 v2, 0x3fb8aa3b, v2
	v_lshlrev_b32_e32 v48, 16, v47
	v_and_b32_e32 v112, 0xffff0000, v47
	v_pk_mov_b32 v[46:47], v[114:115], v[116:117] op_sel:[1,0]
	v_add_f32_e32 v9, v37, v14
	v_exp_f32_e32 v45, v2
	v_sub_f32_e32 v2, v29, v53
	v_pk_mul_f32 v[52:53], v[34:35], v[46:47]
	v_add_f32_e32 v9, v36, v9
	v_add_f32_e32 v9, v53, v9
	v_pk_mul_f32 v[124:125], v[122:123], v[116:117]
	v_add_f32_e32 v9, v52, v9
	v_mul_f32_e32 v36, 0xbfb8aa3b, v9
	v_add_f32_e32 v50, v125, v14
	v_lshlrev_b32_e32 v49, 16, v44
	v_and_b32_e32 v113, 0xffff0000, v44
	v_exp_f32_e32 v44, v36
	v_pk_mul_f32 v[36:37], v[34:35], v[114:115]
	v_add_f32_e32 v50, v124, v50
	v_add_f32_e32 v37, v37, v50
	v_add_f32_e32 v36, v36, v37
	v_mul_f32_e32 v37, 0xbfb8aa3b, v36
	v_exp_f32_e32 v50, v37
	v_mul_f32_e32 v2, 0x3fb8aa3b, v2
	v_exp_f32_e32 v37, v2
	v_add_f32_e32 v2, 1.0, v44
	v_rcp_f32_e32 v44, v2
	v_add_f32_e32 v2, 1.0, v50
	v_pk_mov_b32 v[52:53], v[118:119], v[120:121] op_sel:[1,0]
	v_rcp_f32_e32 v50, v2
	v_mul_f32_e32 v2, v11, v53
	v_pk_add_f32 v[16:17], v[2:3], v[16:17] op_sel_hi:[0,1]
	v_pk_fma_f32 v[16:17], v[10:11], v[52:53], v[16:17]
	v_mul_f32_e32 v36, v36, v50
	v_mul_f32_e32 v2, 0xbfb8aa3b, v16
	v_exp_f32_e32 v2, v2
	v_mov_b32_e32 v17, v3
	v_mul_f32_e32 v9, v9, v44
	v_pk_mul_f32 v[46:47], v[122:123], v[46:47]
	v_add_f32_e32 v2, 1.0, v2
	v_rcp_f32_e32 v50, v2
	v_mul_f32_e32 v2, v11, v119
	v_pk_add_f32 v[18:19], v[2:3], v[18:19] op_sel_hi:[0,1]
	v_pk_fma_f32 v[18:19], v[10:11], v[118:119], v[18:19]
	v_pk_mul_f32 v[116:117], v[122:123], v[114:115]
	v_mul_f32_e32 v2, 0xbfb8aa3b, v18
	v_exp_f32_e32 v19, v2
	v_pk_mul_f32 v[2:3], v[16:17], v[50:51]
	v_and_b32_e32 v51, 0xffff0000, v41
	v_mul_f32_e32 v120, v9, v3
	v_add_f32_e32 v16, 1.0, v19
	v_rcp_f32_e32 v44, v16
	v_mov_b32_e32 v19, v4
	v_mul_f32_e32 v121, v2, v3
	v_fma_f32 v4, v13, v119, v15
	v_pk_mul_f32 v[2:3], v[18:19], v[44:45]
	v_pk_fma_f32 v[16:17], v[12:13], v[118:119], v[4:5] op_sel_hi:[1,1,0]
	v_mul_f32_e32 v125, v2, v3
	v_fma_f32 v2, v13, v53, v15
	s_waitcnt lgkmcnt(0)
	v_sub_f32_e32 v4, v29, v54
	v_mul_f32_e32 v124, v36, v3
	v_pk_fma_f32 v[2:3], v[12:13], v[52:53], v[2:3] op_sel_hi:[1,1,0]
	v_mul_f32_e32 v4, 0x3fb8aa3b, v4
	v_pk_mov_b32 v[52:53], v[48:49], v[114:115] op_sel:[1,0]
	v_add_f32_e32 v9, v47, v14
	v_exp_f32_e32 v19, v4
	v_sub_f32_e32 v4, v29, v55
	v_pk_mul_f32 v[54:55], v[34:35], v[52:53]
	v_add_f32_e32 v9, v46, v9
	v_add_f32_e32 v36, v117, v14
	v_add_f32_e32 v9, v55, v9
	v_pk_mul_f32 v[46:47], v[34:35], v[48:49]
	v_add_f32_e32 v36, v116, v36
	v_add_f32_e32 v9, v54, v9
	v_add_f32_e32 v36, v47, v36
	v_mul_f32_e32 v18, 0xbfb8aa3b, v9
	v_add_f32_e32 v36, v46, v36
	v_lshlrev_b32_e32 v45, 16, v41
	v_exp_f32_e32 v18, v18
	v_mul_f32_e32 v41, 0xbfb8aa3b, v36
	v_exp_f32_e32 v41, v41
	v_mul_f32_e32 v4, 0x3fb8aa3b, v4
	v_exp_f32_e32 v47, v4
	v_add_f32_e32 v4, 1.0, v18
	v_rcp_f32_e32 v18, v4
	v_add_f32_e32 v4, 1.0, v41
	v_pk_mov_b32 v[54:55], v[112:113], v[118:119] op_sel:[1,0]
	v_rcp_f32_e32 v41, v4
	v_mul_f32_e32 v4, v11, v55
	v_pk_add_f32 v[2:3], v[4:5], v[2:3] op_sel_hi:[0,1]
	v_pk_fma_f32 v[2:3], v[10:11], v[54:55], v[2:3]
	v_mul_f32_e32 v4, v11, v113
	v_mul_f32_e32 v3, 0xbfb8aa3b, v2
	v_exp_f32_e32 v3, v3
	v_pk_add_f32 v[16:17], v[4:5], v[16:17] op_sel_hi:[0,1]
	v_pk_fma_f32 v[16:17], v[10:11], v[112:113], v[16:17]
	v_mul_f32_e32 v41, v36, v41
	v_add_f32_e32 v3, 1.0, v3
	v_rcp_f32_e32 v36, v3
	v_mul_f32_e32 v3, 0xbfb8aa3b, v16
	v_exp_f32_e32 v4, v3
	v_mul_f32_e32 v9, v9, v18
	v_lshlrev_b32_e32 v44, 16, v43
	v_pk_mul_f32 v[52:53], v[122:123], v[52:53]
	v_add_f32_e32 v4, 1.0, v4
	v_rcp_f32_e32 v18, v4
	v_mov_b32_e32 v3, v5
	v_pk_mul_f32 v[2:3], v[2:3], v[36:37]
	v_mov_b32_e32 v17, v6
	v_pk_mov_b32 v[4:5], v[44:45], v[48:49] op_sel:[1,0]
	v_add_f32_e32 v6, v53, v14
	v_and_b32_e32 v50, 0xffff0000, v43
	v_mul_f32_e32 v43, v9, v3
	v_mul_f32_e32 v116, v2, v3
	v_pk_mul_f32 v[2:3], v[16:17], v[18:19]
	v_pk_mul_f32 v[16:17], v[34:35], v[4:5]
	v_add_f32_e32 v6, v52, v6
	v_add_f32_e32 v6, v17, v6
	v_add_f32_e32 v9, v16, v6
	v_mul_f32_e32 v6, 0xbfb8aa3b, v9
	v_exp_f32_e32 v6, v6
	v_pk_mul_f32 v[114:115], v[122:123], v[48:49]
	v_mul_f32_e32 v41, v41, v3
	v_mul_f32_e32 v48, v2, v3
	v_add_f32_e32 v3, 1.0, v6
	v_rcp_f32_e32 v18, v3
	v_fma_f32 v2, v13, v55, v15
	v_fma_f32 v6, v13, v113, v15
	v_pk_fma_f32 v[2:3], v[12:13], v[54:55], v[2:3] op_sel_hi:[1,1,0]
	v_mul_f32_e32 v9, v9, v18
	v_pk_mov_b32 v[18:19], v[50:51], v[112:113] op_sel:[1,0]
	v_pk_fma_f32 v[16:17], v[12:13], v[112:113], v[6:7] op_sel_hi:[1,1,0]
	v_mul_f32_e32 v6, v11, v19
	v_pk_add_f32 v[2:3], v[6:7], v[2:3] op_sel_hi:[0,1]
	v_pk_fma_f32 v[2:3], v[10:11], v[18:19], v[2:3]
	v_add_f32_e32 v6, v115, v14
	v_mul_f32_e32 v3, 0xbfb8aa3b, v2
	v_exp_f32_e32 v3, v3
	v_pk_mul_f32 v[36:37], v[34:35], v[44:45]
	v_add_f32_e32 v6, v114, v6
	v_pk_mul_f32 v[4:5], v[122:123], v[4:5]
	v_add_f32_e32 v3, 1.0, v3
	v_rcp_f32_e32 v46, v3
	v_add_f32_e32 v3, v37, v6
	v_add_f32_e32 v36, v36, v3
	v_mov_b32_e32 v3, v7
	v_mul_f32_e32 v6, v11, v51
	v_pk_mul_f32 v[2:3], v[2:3], v[46:47]
	v_pk_add_f32 v[6:7], v[6:7], v[16:17] op_sel_hi:[0,1]
	v_mul_f32_e32 v37, v9, v3
	v_pk_fma_f32 v[6:7], v[10:11], v[50:51], v[6:7]
	v_mul_f32_e32 v9, 0xbfb8aa3b, v36
	v_exp_f32_e32 v9, v9
	v_mul_f32_e32 v16, 0xbfb8aa3b, v6
	v_exp_f32_e32 v16, v16
	v_sub_f32_e32 v7, v29, v56
	v_mul_f32_e32 v7, 0x3fb8aa3b, v7
	v_exp_f32_e32 v17, v7
	v_add_f32_e32 v7, 1.0, v9
	v_rcp_f32_e32 v7, v7
	v_add_f32_e32 v9, 1.0, v16
	v_rcp_f32_e32 v16, v9
	v_mul_f32_e32 v45, v2, v3
	v_mul_f32_e32 v9, v36, v7
	v_mov_b32_e32 v7, v8
	v_pk_mul_f32 v[2:3], v[6:7], v[16:17]
	v_lshlrev_b32_e32 v8, 16, v39
	v_mul_f32_e32 v16, v9, v3
	v_mov_b32_e32 v9, v44
	v_add_f32_e32 v5, v5, v14
	v_pk_mul_f32 v[8:9], v[34:35], v[8:9]
	v_add_f32_e32 v4, v4, v5
	v_fma_f32 v6, v13, v19, v15
	v_add_f32_e32 v4, v9, v4
	v_pk_fma_f32 v[6:7], v[12:13], v[18:19], v[6:7] op_sel_hi:[1,1,0]
	v_add_f32_e32 v13, v8, v4
	ds_read2st64_b32 v[8:9], v88 offset1:16
	v_mul_f32_e32 v12, v11, v50
	v_and_b32_e32 v4, 0xffff0000, v39
	v_mov_b32_e32 v5, v50
	v_pk_add_f32 v[6:7], v[12:13], v[6:7] op_sel_hi:[0,1]
	v_pk_fma_f32 v[4:5], v[10:11], v[4:5], v[6:7]
	v_mul_f32_e32 v6, 0xbfb8aa3b, v13
	v_exp_f32_e32 v6, v6
	v_mul_f32_e32 v7, 0xbfb8aa3b, v4
	s_waitcnt lgkmcnt(0)
	v_sub_f32_e32 v5, v29, v9
	v_exp_f32_e32 v9, v7
	v_mul_f32_e32 v5, 0x3fb8aa3b, v5
	s_lshr_b32 s39, s55, 3
	v_exp_f32_e32 v7, v5
	v_add_f32_e32 v5, 1.0, v6
	s_and_b32 s39, s39, 63
	v_rcp_f32_e32 v5, v5
	v_add_f32_e32 v6, 1.0, v9
	s_lshl_b32 s58, s39, 7
	v_rcp_f32_e32 v6, v6
	s_add_i32 s58, s58, s41
	v_add_u32_e32 v18, s58, v67
	v_mul_f32_e32 v10, v13, v5
	v_mov_b32_e32 v5, v8
	s_lshl_b32 s60, s40, 6
	s_lshl_b32 s59, s40, 12
	v_mad_i64_i32 v[18:19], s[40:41], v18, s45, v[20:21]
	v_mul_f32_e32 v9, v2, v3
	v_pk_mul_f32 v[2:3], v[4:5], v[6:7]
	v_lshl_add_u64 v[34:35], v[18:19], 0, s[34:35]
	v_add_u32_e32 v18, s58, v23
	v_mul_f32_e32 v5, v10, v3
	v_mul_f32_e32 v10, v2, v3
	v_cvt_pk_bf16_f32 v2, v57, v120
	v_cvt_pk_bf16_f32 v3, v124, v43
	v_cvt_pk_bf16_f32 v4, v41, v37
	v_mad_i64_i32 v[36:37], s[40:41], v18, s45, v[20:21]
	v_add_u32_e32 v18, s58, v38
	v_mad_i64_i32 v[18:19], s[40:41], v18, s45, v[20:21]
	v_lshl_add_u64 v[38:39], v[18:19], 0, s[34:35]
	v_add_u32_e32 v18, s58, v40
	v_mad_i64_i32 v[18:19], s[40:41], v18, s45, v[20:21]
	v_lshl_add_u64 v[40:41], v[18:19], 0, s[34:35]
	v_add_u32_e32 v18, s58, v42
	s_lshl_b32 s42, s43, 3
	s_lshl_b32 s43, s39, 6
	v_mad_i64_i32 v[18:19], s[40:41], v18, s45, v[20:21]
	s_or_b32 s40, s59, s43
	s_or_b32 s40, s40, s42
	s_ashr_i32 s41, s40, 31
	v_cvt_pk_bf16_f32 v5, v16, v5
	s_lshl_b64 s[40:41], s[40:41], 2
	v_readlane_b32 s61, v253, 19
	v_cvt_pk_bf16_f32 v6, v126, v121
	v_cvt_pk_bf16_f32 v7, v125, v116
	v_cvt_pk_bf16_f32 v8, v48, v45
	v_cvt_pk_bf16_f32 v9, v9, v10
	ds_write_b128 v91, v[2:5] offset:43008
	ds_write_b128 v91, v[6:9] offset:43280
	s_add_u32 s58, s40, 0x66000000
	ds_read_b128 v[14:17], v106 offset:8192
	ds_read_b128 v[10:13], v106 offset:8256
	ds_read_b128 v[6:9], v106 offset:8320
	ds_read_b128 v[2:5], v106 offset:8384
	s_addc_u32 s61, s41, 0
	s_or_b32 s40, s60, s39
	s_ashr_i32 s41, s40, 31
	s_lshl_b64 s[40:41], s[40:41], 12
	v_lshl_add_u64 v[42:43], v[18:19], 0, s[34:35]
	v_or_b32_e32 v18, s40, v22
	v_mov_b32_e32 v19, s41
	v_or_b32_e32 v18, s38, v18
	v_readlane_b32 s62, v253, 20
	v_lshlrev_b64 v[18:19], 8, v[18:19]
	s_mov_b32 s26, 0
	v_lshl_add_u64 v[44:45], v[26:27], 0, v[18:19]
	s_mov_b64 s[38:39], 0
	s_mov_b32 s62, 0
	v_readlane_b32 s63, v253, 21
	v_readlane_b32 s64, v253, 22
	v_readlane_b32 s65, v253, 23
	v_readlane_b32 s66, v253, 24
	v_readlane_b32 s67, v253, 25
	v_readlane_b32 s68, v253, 26
	v_readlane_b32 s69, v253, 27
	v_readlane_b32 s72, v253, 30
	v_readlane_b32 s73, v253, 31
	v_readlane_b32 s74, v253, 32
	v_readlane_b32 s75, v253, 33
	s_waitcnt vmcnt(0)
	ds_write_b64 v232, v[234:235]
	ds_write_b64 v232, v[238:239] offset:256
	ds_write_b64 v233, v[236:237] offset:512
	s_mov_b32 s76, 0x45c00000
	s_mov_b32 s77, 0
	s_movk_i32 s78, 0x3000
	s_mov_b32 s79, 0
	s_movk_i32 s80, 0x6000
	s_mov_b32 s81, 0
	v_lshl_add_u64 v[190:191], s[92:93], 0, v[42:43]
	v_lshl_add_u64 v[192:193], s[92:93], 0, v[40:41]
	v_lshl_add_u64 v[194:195], s[92:93], 0, v[38:39]
	v_lshl_add_u64 v[196:197], s[92:93], 0, v[36:37]
	global_load_dword v168, v[190:191], off
	global_load_dword v169, v[192:193], off
	global_load_dword v170, v[194:195], off
	v_lshl_add_u64 v[196:197], v[196:197], 0, s[76:77]
	global_load_dword v171, v[196:197], off offset:128
	v_lshl_add_u64 v[196:197], v[196:197], 0, s[78:79]
	global_load_dword v172, v[196:197], off offset:128
	v_lshl_add_u64 v[196:197], v[196:197], 0, s[78:79]
	global_load_dword v173, v[196:197], off offset:128
	v_lshl_add_u64 v[196:197], v[196:197], 0, s[78:79]
	global_load_dword v174, v[196:197], off offset:128
	v_lshl_add_u64 v[196:197], v[196:197], 0, s[78:79]
	global_load_dword v175, v[196:197], off offset:128
	v_lshl_add_u64 v[196:197], v[196:197], 0, s[78:79]
	global_load_dword v176, v[196:197], off offset:128
	v_lshl_add_u64 v[196:197], v[196:197], 0, s[78:79]
	global_load_dword v177, v[196:197], off offset:128
	v_lshl_add_u64 v[190:191], s[92:93], 0, v[34:35]
	global_load_dword v178, v[190:191], off
	s_waitcnt lgkmcnt(0)
	s_barrier
	s_bitcmp1_b32 s84, 1
	s_cbranch_scc1 .Lq_402
	s_branch .LBB0_403

.Lq_402:
	s_cmp_lt_u32 s62, 2
	s_cbranch_scc1 .Lq_w0
	s_waitcnt vmcnt(2)
	s_branch .Lq_wd

.Lq_pf_skip:
	v_mov_b32_e32 v119, s26
	ds_read_b32 v29, v119 offset:5116
	v_add_u32_e32 v112, s26, v87
	ds_read2st64_b32 v[142:143], v112 offset0:2 offset1:18
	v_add_u32_e32 v119, s26, v104
	ds_read_b128 v[144:147], v119 offset:512
	ds_read_b128 v[112:115], v119 offset:4608
	ds_read_b96 v[116:118], v119 offset:528
	ds_read_b96 v[18:20], v119 offset:4624
	s_waitcnt lgkmcnt(0)
	v_sub_f32_e32 v112, v29, v112
	v_sub_f32_e32 v113, v29, v113
	v_sub_f32_e32 v114, v29, v114
	v_sub_f32_e32 v115, v29, v115
	v_sub_f32_e32 v18, v29, v18
	v_sub_f32_e32 v19, v29, v19
	v_sub_f32_e32 v20, v29, v20
	v_sub_f32_e32 v143, v29, v143
	v_mul_f32_e32 v112, 0x3fb8aa3b, v112
	v_mul_f32_e32 v113, 0x3fb8aa3b, v113
	v_mul_f32_e32 v114, 0x3fb8aa3b, v114
	v_mul_f32_e32 v115, 0x3fb8aa3b, v115
	v_mul_f32_e32 v18, 0x3fb8aa3b, v18
	v_mul_f32_e32 v19, 0x3fb8aa3b, v19
	v_mul_f32_e32 v20, 0x3fb8aa3b, v20
	v_mul_f32_e32 v143, 0x3fb8aa3b, v143
	v_exp_f32_e32 v112, v112
	v_exp_f32_e32 v113, v113
	v_exp_f32_e32 v114, v114
	v_exp_f32_e32 v115, v115
	v_exp_f32_e32 v18, v18
	v_exp_f32_e32 v19, v19
	v_exp_f32_e32 v20, v20
	v_exp_f32_e32 v143, v143
	v_mul_f32_e32 v144, v144, v112
	v_mul_f32_e32 v145, v145, v113
	v_mul_f32_e32 v146, v146, v114
	v_mul_f32_e32 v147, v147, v115
	v_mul_f32_e32 v116, v116, v18
	v_mul_f32_e32 v117, v117, v19
	v_mul_f32_e32 v118, v118, v20
	v_mul_f32_e32 v142, v142, v143
	v_fma_f32 v112, v48, v120, v50
	v_fma_f32 v113, v49, v131, v51
	v_fmac_f32_e32 v112, v56, v121
	v_fmac_f32_e32 v113, v57, v132
	v_fmac_f32_e32 v112, v46, v122
	v_fmac_f32_e32 v113, v47, v133
	v_fmac_f32_e32 v112, v54, v123
	v_fmac_f32_e32 v113, v55, v134
	v_mul_f32_e32 v114, 0xbfb8aa3b, v112
	v_mul_f32_e32 v115, 0xbfb8aa3b, v113
	v_exp_f32_e32 v114, v114
	v_exp_f32_e32 v115, v115
	v_add_f32_e32 v114, 1.0, v114
	v_add_f32_e32 v115, 1.0, v115
	v_rcp_f32_e32 v114, v114
	v_rcp_f32_e32 v115, v115
	v_mul_f32_e32 v112, v112, v144
	v_mul_f32_e32 v113, v113, v144
	v_mul_f32_e32 v120, v112, v114
	v_mul_f32_e32 v131, v113, v115
	v_fma_f32 v112, v48, v121, v50
	v_fma_f32 v113, v49, v132, v51
	v_fmac_f32_e32 v112, v56, v122
	v_fmac_f32_e32 v113, v57, v133
	v_fmac_f32_e32 v112, v46, v123
	v_fmac_f32_e32 v113, v47, v134
	v_fmac_f32_e32 v112, v54, v124
	v_fmac_f32_e32 v113, v55, v135
	v_mul_f32_e32 v114, 0xbfb8aa3b, v112
	v_mul_f32_e32 v115, 0xbfb8aa3b, v113
	v_exp_f32_e32 v114, v114
	v_exp_f32_e32 v115, v115
	v_add_f32_e32 v114, 1.0, v114
	v_add_f32_e32 v115, 1.0, v115
	v_rcp_f32_e32 v114, v114
	v_rcp_f32_e32 v115, v115
	v_mul_f32_e32 v112, v112, v145
	v_mul_f32_e32 v113, v113, v145
	v_mul_f32_e32 v121, v112, v114
	v_mul_f32_e32 v132, v113, v115
	v_fma_f32 v112, v48, v122, v50
	v_fma_f32 v113, v49, v133, v51
	v_fmac_f32_e32 v112, v56, v123
	v_fmac_f32_e32 v113, v57, v134
	v_fmac_f32_e32 v112, v46, v124
	v_fmac_f32_e32 v113, v47, v135
	v_fmac_f32_e32 v112, v54, v125
	v_fmac_f32_e32 v113, v55, v136
	v_mul_f32_e32 v114, 0xbfb8aa3b, v112
	v_mul_f32_e32 v115, 0xbfb8aa3b, v113
	v_exp_f32_e32 v114, v114
	v_exp_f32_e32 v115, v115
	v_add_f32_e32 v114, 1.0, v114
	v_add_f32_e32 v115, 1.0, v115
	v_rcp_f32_e32 v114, v114
	v_rcp_f32_e32 v115, v115
	v_mul_f32_e32 v112, v112, v146
	v_mul_f32_e32 v113, v113, v146
	v_mul_f32_e32 v122, v112, v114
	v_mul_f32_e32 v133, v113, v115
	v_fma_f32 v112, v48, v123, v50
	v_fma_f32 v113, v49, v134, v51
	v_fmac_f32_e32 v112, v56, v124
	v_fmac_f32_e32 v113, v57, v135
	v_fmac_f32_e32 v112, v46, v125
	v_fmac_f32_e32 v113, v47, v136
	v_fmac_f32_e32 v112, v54, v126
	v_fmac_f32_e32 v113, v55, v137
	v_mul_f32_e32 v114, 0xbfb8aa3b, v112
	v_mul_f32_e32 v115, 0xbfb8aa3b, v113
	v_exp_f32_e32 v114, v114
	v_exp_f32_e32 v115, v115
	v_add_f32_e32 v114, 1.0, v114
	v_add_f32_e32 v115, 1.0, v115
	v_rcp_f32_e32 v114, v114
	v_rcp_f32_e32 v115, v115
	v_mul_f32_e32 v112, v112, v147
	v_mul_f32_e32 v113, v113, v147
	v_mul_f32_e32 v123, v112, v114
	v_mul_f32_e32 v134, v113, v115
	v_fma_f32 v112, v48, v124, v50
	v_fma_f32 v113, v49, v135, v51
	v_fmac_f32_e32 v112, v56, v125
	v_fmac_f32_e32 v113, v57, v136
	v_fmac_f32_e32 v112, v46, v126
	v_fmac_f32_e32 v113, v47, v137
	v_fmac_f32_e32 v112, v54, v127
	v_fmac_f32_e32 v113, v55, v138
	v_mul_f32_e32 v114, 0xbfb8aa3b, v112
	v_mul_f32_e32 v115, 0xbfb8aa3b, v113
	v_exp_f32_e32 v114, v114
	v_exp_f32_e32 v115, v115
	v_add_f32_e32 v114, 1.0, v114
	v_add_f32_e32 v115, 1.0, v115
	v_rcp_f32_e32 v114, v114
	v_rcp_f32_e32 v115, v115
	v_mul_f32_e32 v112, v112, v116
	v_mul_f32_e32 v113, v113, v116
	v_mul_f32_e32 v124, v112, v114
	v_mul_f32_e32 v135, v113, v115
	v_fma_f32 v112, v48, v125, v50
	v_fma_f32 v113, v49, v136, v51
	v_fmac_f32_e32 v112, v56, v126
	v_fmac_f32_e32 v113, v57, v137
	v_fmac_f32_e32 v112, v46, v127
	v_fmac_f32_e32 v113, v47, v138
	v_fmac_f32_e32 v112, v54, v128
	v_fmac_f32_e32 v113, v55, v139
	v_mul_f32_e32 v114, 0xbfb8aa3b, v112
	v_mul_f32_e32 v115, 0xbfb8aa3b, v113
	v_exp_f32_e32 v114, v114
	v_exp_f32_e32 v115, v115
	v_add_f32_e32 v114, 1.0, v114
	v_add_f32_e32 v115, 1.0, v115
	v_rcp_f32_e32 v114, v114
	v_rcp_f32_e32 v115, v115
	v_mul_f32_e32 v112, v112, v117
	v_mul_f32_e32 v113, v113, v117
	v_mul_f32_e32 v125, v112, v114
	v_mul_f32_e32 v136, v113, v115
	v_fma_f32 v112, v48, v126, v50
	v_fma_f32 v113, v49, v137, v51
	v_fmac_f32_e32 v112, v56, v127
	v_fmac_f32_e32 v113, v57, v138
	v_fmac_f32_e32 v112, v46, v128
	v_fmac_f32_e32 v113, v47, v139
	v_fmac_f32_e32 v112, v54, v129
	v_fmac_f32_e32 v113, v55, v140
	v_mul_f32_e32 v114, 0xbfb8aa3b, v112
	v_mul_f32_e32 v115, 0xbfb8aa3b, v113
	v_exp_f32_e32 v114, v114
	v_exp_f32_e32 v115, v115
	v_add_f32_e32 v114, 1.0, v114
	v_add_f32_e32 v115, 1.0, v115
	v_rcp_f32_e32 v114, v114
	v_rcp_f32_e32 v115, v115
	v_mul_f32_e32 v112, v112, v118
	v_mul_f32_e32 v113, v113, v118
	v_mul_f32_e32 v126, v112, v114
	v_mul_f32_e32 v137, v113, v115
	v_fma_f32 v112, v48, v127, v50
	v_fma_f32 v113, v49, v138, v51
	v_fmac_f32_e32 v112, v56, v128
	v_fmac_f32_e32 v113, v57, v139
	v_fmac_f32_e32 v112, v46, v129
	v_fmac_f32_e32 v113, v47, v140
	v_fmac_f32_e32 v112, v54, v130
	v_fmac_f32_e32 v113, v55, v141
	v_mul_f32_e32 v114, 0xbfb8aa3b, v112
	v_mul_f32_e32 v115, 0xbfb8aa3b, v113
	v_exp_f32_e32 v114, v114
	v_exp_f32_e32 v115, v115
	v_add_f32_e32 v114, 1.0, v114
	v_add_f32_e32 v115, 1.0, v115
	v_rcp_f32_e32 v114, v114
	v_rcp_f32_e32 v115, v115
	v_mul_f32_e32 v112, v112, v142
	v_mul_f32_e32 v113, v113, v142
	v_mul_f32_e32 v127, v112, v114
	v_mul_f32_e32 v138, v113, v115
	s_bitcmp0_b32 s62, 0
	s_cselect_b64 s[40:41], -1, 0
	s_and_b64 s[40:41], s[40:41], exec
	s_mov_b32 s40, 0xec00
	s_cselect_b32 s40, s40, 0xa800
	s_add_i32 s40, s40, 0
	v_cvt_pk_bf16_f32 v46, v120, v121
	v_cvt_pk_bf16_f32 v47, v122, v123
	v_cvt_pk_bf16_f32 v48, v124, v125
	v_cvt_pk_bf16_f32 v49, v126, v127
	v_cvt_pk_bf16_f32 v50, v131, v132
	v_cvt_pk_bf16_f32 v51, v133, v134
	v_cvt_pk_bf16_f32 v52, v135, v136
	v_cvt_pk_bf16_f32 v53, v137, v138
	v_add3_u32 v18, s40, v89, v90
	ds_write_b128 v18, v[46:49]
	ds_write_b128 v18, v[50:53] offset:272
	s_cmp_eq_u32 s62, 0
	s_cbranch_scc1 .Lp2_nofl_c
	s_and_b32 s76, s62, 1
	s_xor_b32 s76, s76, 1
	s_mul_i32 s76, s76, 0x4400
	v_add_u32_e32 v216, s76, v213
	ds_read_b128 v[198:201], v216
	ds_read_b128 v[202:205], v216 offset:1088
	v_lshl_add_u64 v[206:207], s[92:93], 0, v[44:45]
	v_lshl_add_u64 v[206:207], v[206:207], 0, v[214:215]
	s_mov_b32 s76, 0x5dffb000
	s_mov_b32 s77, 0
	v_lshl_add_u64 v[206:207], v[206:207], 0, s[76:77]

.Lq_post:
	s_or_b64 exec, exec, s[42:43]
	s_add_i32 s62, s62, 1
	s_add_u32 s38, s38, 0x100
	s_addc_u32 s39, s39, 0
	s_addk_i32 s26, 0x200
	s_add_u32 s58, s58, 4
	s_addc_u32 s61, s61, 0
	s_mov_b64 s[40:41], 0x4000
	v_lshl_add_u64 v[44:45], v[44:45], 0, s[40:41]
	s_cmpk_eq_i32 s38, 0x700
	s_waitcnt lgkmcnt(0)
	s_barrier
	s_cbranch_scc1 .LBB0_405
	s_branch .Lq_402
